# speedup vs baseline: 1.0198x; 1.0198x over previous
_Z8moe_gemmILi1EEvPKDF16_S1_PvPKyPKiPKfS1_:
	s_load_dwordx2 s[4:5], s[0:1], 0x18
	s_load_dwordx2 s[8:9], s[0:1], 0x20
	v_and_b32_e32 v1, 15, v0
	v_lshrrev_b32_e32 v2, 2, v1
	v_and_b32_e32 v3, 3, v1
	v_lshlrev_b32_e32 v2, 7, v2
	v_lshl_add_u32 v2, v3, 1, v2
	s_mov_b32 s10, 0x1c71c72
	s_mov_b32 s11, 0x199999a
	s_waitcnt lgkmcnt(0)
	global_load_ushort v4, v2, s[4:5] offset:512
	s_waitcnt vmcnt(0)
	s_load_dwordx4 s[4:7], s[0:1], 0x0
	v_add_u32_e32 v5, 0x8f, v4
	v_add_u32_e32 v6, 0x9f, v4
	v_mul_hi_u32 v5, v5, s10
	v_mul_hi_u32 v6, v6, s11
	v_mov_b32_e32 v7, v5
	v_mov_b32_e32 v8, v6
	s_nop 1
	v_add_u32_dpp v7, v7, v7 row_shr:1 row_mask:0xf bank_mask:0xf
	v_add_u32_dpp v8, v8, v8 row_shr:1 row_mask:0xf bank_mask:0xf
	s_nop 1
	v_add_u32_dpp v7, v7, v7 row_shr:2 row_mask:0xf bank_mask:0xf
	v_add_u32_dpp v8, v8, v8 row_shr:2 row_mask:0xf bank_mask:0xf
	s_nop 1
	v_add_u32_dpp v7, v7, v7 row_shr:4 row_mask:0xf bank_mask:0xf
	v_add_u32_dpp v8, v8, v8 row_shr:4 row_mask:0xf bank_mask:0xf
	s_nop 1
	v_add_u32_dpp v7, v7, v7 row_shr:8 row_mask:0xf bank_mask:0xf
	v_add_u32_dpp v8, v8, v8 row_shr:8 row_mask:0xf bank_mask:0xf
	s_nop 1
	v_readlane_b32 s14, v7, 15
	v_readlane_b32 s15, v8, 15
	s_cmpk_lt_u32 s14, 0x41
	s_cselect_b64 s[10:11], -1, 0
	s_cselect_b32 s16, s14, s15
	s_lshl_b32 s17, s16, 2
	s_cmp_ge_i32 s2, s17
	s_cbranch_scc1 .LBB3_175
	s_lshr_b32 s20, s16, 1
	s_and_b32 s21, s17, 4
	s_and_b32 s22, s2, 7
	s_add_i32 s23, s20, 1
	s_min_u32 s24, s22, s21
	s_mul_i32 s24, s24, s23
	s_sub_i32 s25, s22, s21
	s_max_i32 s25, s25, 0
	s_mul_i32 s25, s25, s20
	s_add_i32 s18, s24, s25
	s_ashr_i32 s27, s2, 3
	s_add_i32 s18, s18, s27
	s_ashr_i32 s19, s18, 2
	v_cndmask_b32_e64 v9, v6, v5, s[10:11]
	v_cndmask_b32_e64 v10, v8, v7, s[10:11]
	v_sub_u32_e32 v11, v10, v9
	v_cmp_le_i32_e64 s[28:29], v11, s19
	v_cmp_gt_i32_e64 s[30:31], v10, s19
	s_and_b64 s[28:29], s[28:29], s[30:31]
	s_ff1_i32_b64 s13, s[28:29]
	v_readlane_b32 s12, v4, s13
	v_readlane_b32 s26, v9, s13
	v_readlane_b32 s27, v11, s13
	s_sub_i32 s2, s19, s27

_Z8moe_gemmILi2EEvPKDF16_S1_PvPKyPKiPKfS1_:
	s_load_dwordx2 s[4:5], s[0:1], 0x18
	s_load_dwordx2 s[8:9], s[0:1], 0x20
	v_and_b32_e32 v1, 15, v0
	v_lshrrev_b32_e32 v2, 2, v1
	v_and_b32_e32 v3, 3, v1
	v_lshlrev_b32_e32 v2, 7, v2
	v_lshl_add_u32 v2, v3, 1, v2
	s_mov_b32 s10, 0x1c71c72
	s_mov_b32 s11, 0x199999a
	s_waitcnt lgkmcnt(0)
	global_load_ushort v4, v2, s[4:5] offset:0
	s_waitcnt vmcnt(0)
	s_load_dwordx4 s[4:7], s[0:1], 0x0
	v_add_u32_e32 v5, 0x8f, v4
	v_add_u32_e32 v6, 0x9f, v4
	v_mul_hi_u32 v5, v5, s10
	v_mul_hi_u32 v6, v6, s11
	v_mov_b32_e32 v7, v5
	v_mov_b32_e32 v8, v6
	s_nop 1
	v_add_u32_dpp v7, v7, v7 row_shr:1 row_mask:0xf bank_mask:0xf
	v_add_u32_dpp v8, v8, v8 row_shr:1 row_mask:0xf bank_mask:0xf
	s_nop 1
	v_add_u32_dpp v7, v7, v7 row_shr:2 row_mask:0xf bank_mask:0xf
	v_add_u32_dpp v8, v8, v8 row_shr:2 row_mask:0xf bank_mask:0xf
	s_nop 1
	v_add_u32_dpp v7, v7, v7 row_shr:4 row_mask:0xf bank_mask:0xf
	v_add_u32_dpp v8, v8, v8 row_shr:4 row_mask:0xf bank_mask:0xf
	s_nop 1
	v_add_u32_dpp v7, v7, v7 row_shr:8 row_mask:0xf bank_mask:0xf
	v_add_u32_dpp v8, v8, v8 row_shr:8 row_mask:0xf bank_mask:0xf
	s_nop 1
	v_readlane_b32 s14, v7, 15
	v_readlane_b32 s15, v8, 15
	s_cmpk_lt_u32 s14, 0x41
	s_cselect_b64 s[10:11], -1, 0
	s_cselect_b32 s16, s14, s15
	s_lshl_b32 s17, s16, 2
	s_cmp_ge_i32 s2, s17
	s_cbranch_scc1 .LBB4_181
	s_lshr_b32 s20, s16, 1
	s_and_b32 s21, s17, 4
	s_and_b32 s22, s2, 7
	s_add_i32 s23, s20, 1
	s_min_u32 s24, s22, s21
	s_mul_i32 s24, s24, s23
	s_sub_i32 s25, s22, s21
	s_max_i32 s25, s25, 0
	s_mul_i32 s25, s25, s20
	s_add_i32 s18, s24, s25
	s_ashr_i32 s27, s2, 3
	s_add_i32 s18, s18, s27
	s_ashr_i32 s19, s18, 2
	v_cndmask_b32_e64 v9, v6, v5, s[10:11]
	v_cndmask_b32_e64 v10, v8, v7, s[10:11]
	v_sub_u32_e32 v11, v10, v9
	v_cmp_le_i32_e64 s[28:29], v11, s19
	v_cmp_gt_i32_e64 s[30:31], v10, s19
	s_and_b64 s[28:29], s[28:29], s[30:31]
	s_ff1_i32_b64 s13, s[28:29]
	v_readlane_b32 s12, v4, s13
	v_readlane_b32 s26, v9, s13
	v_readlane_b32 s27, v11, s13
	s_sub_i32 s2, s19, s27
